# speedup vs baseline: 1.0293x; 1.0027x over previous
_Z16sum_layer_kernelPKfS0_Pf:
	s_load_dwordx4 s[4:7], s[0:1], 0x0
	s_load_dwordx2 s[8:9], s[0:1], 0x10
	s_cmp_lt_u32 s2, 0x100
	s_cbranch_scc0 .Lkeep_low_prio
	s_setprio 3
.Lkeep_low_prio:
	v_lshrrev_b32_e32 v42, 6, v0
	v_bfe_u32 v41, v0, 5, 1
	v_and_b32_e32 v40, 31, v0
	v_readfirstlane_b32 s23, v42
	v_and_b32_e32 v43, 7, v0
	v_bfe_u32 v44, v0, 3, 3
	s_lshl_b32 s3, s2, 12
	s_lshl_b32 s19, s2, 7
	s_lshl_b32 s23, s23, 12
	v_lshlrev_b32_e32 v1, 11, v41
	v_lshl_or_b32 v1, v40, 2, v1
	s_mov_b32 m0, s23
	v_lshrrev_b32_e32 v46, 1, v44
	v_xor_b32_e32 v46, v43, v46
	v_lshlrev_b32_e32 v46, 4, v46
	v_lshl_add_u32 v35, v44, 16, v46
	v_lshl_add_u32 v35, v42, 21, v35
	v_add_u32_e32 v35, s19, v35
	v_xor_b32_e32 v86, 64, v35
	s_mov_b32 s20, 0x7fc00
	s_mov_b32 s21, 0xff800
	s_mov_b32 s22, 0x17f400
	s_mov_b32 s14, 0x200000
	s_mov_b32 s15, 0x20000
	v_and_b32_e32 v45, 63, v0
	v_lshlrev_b32_e32 v37, 4, v45
	s_add_u32 s54, s23, 0x4000
	s_waitcnt lgkmcnt(0)
	s_mov_b32 s12, s6
	s_and_b32 s13, s7, 0xffff
	s_and_b32 s5, s5, 0xffff
	s_mov_b32 s6, 0x800000
	s_mov_b32 s7, s15
	s_mov_b32 m0, s54
	s_nop 0
	buffer_load_dwordx4 v37, s[12:15], s3 offen nt lds
	buffer_load_dwordx4 v37, s[12:15], s3 offen offset:1024 nt lds
	buffer_load_dwordx4 v37, s[12:15], s3 offen offset:2048 nt lds
	buffer_load_dwordx4 v37, s[12:15], s3 offen offset:3072 nt lds
	s_mov_b32 m0, s23
	s_nop 0
	buffer_load_dwordx4 v35, s[4:7], 0 offen nt lds
	buffer_load_dwordx4 v86, s[4:7], s20 offen offset:1024 nt lds
	buffer_load_dwordx4 v35, s[4:7], s21 offen offset:2048 nt lds
	buffer_load_dwordx4 v86, s[4:7], s22 offen offset:3072 nt lds
	v_and_b32_e32 v45, 63, v0
	v_lshlrev_b32_e32 v36, 2, v40
	v_lshl_add_u32 v36, v41, 18, v36
	v_lshl_add_u32 v36, v42, 21, v36
	v_add_u32_e32 v36, s19, v36
	v_bfe_u32 v47, v40, 1, 3
	v_lshlrev_b32_e32 v39, 2, v41
	v_xor_b32_e32 v39, v39, v47
	v_lshlrev_b32_e32 v39, 4, v39
	v_lshl_add_u32 v39, v40, 7, v39
	v_lshl_add_u32 v39, v42, 12, v39
	v_xor_b32_e32 v81, 16, v39
	v_xor_b32_e32 v82, 32, v39
	v_xor_b32_e32 v83, 48, v39
	v_cmp_gt_u32_e32 vcc, 32, v45
	v_mov_b32_e32 v34, 0xc1600000
	v_mov_b32_e32 v84, 0x3fb8aa3b
	v_mov_b32_e32 v85, 0x3f317218
	s_lshl_b32 s24, 1, 16
	s_lshl_b32 s25, 2, 16
	s_lshl_b32 s26, 3, 16
	s_lshl_b32 s27, 8, 16
	s_lshl_b32 s28, 9, 16
	s_lshl_b32 s29, 10, 16
	s_lshl_b32 s30, 11, 16
	s_lshl_b32 s31, 16, 16
	s_lshl_b32 s32, 17, 16
	s_lshl_b32 s33, 18, 16
	s_lshl_b32 s34, 19, 16
	s_lshl_b32 s35, 24, 16
	s_lshl_b32 s36, 25, 16
	s_lshl_b32 s37, 26, 16
	s_lshl_b32 s38, 27, 16
	s_and_b32 s9, s9, 0xffff
	s_mov_b32 s10, s6
	s_mov_b32 s11, s15
	v_lshl_add_u32 v38, v42, 12, v1
	v_add_u32_e32 v38, 0x4000, v38
	v_add_u32_e32 v87, 0x400, v38
	s_waitcnt vmcnt(4)
	ds_read2_b32 v[18:19], v38 offset0:0 offset1:32
	ds_read2_b32 v[20:21], v38 offset0:64 offset1:96
	ds_read2_b32 v[22:23], v38 offset0:128 offset1:160
	ds_read2_b32 v[24:25], v38 offset0:192 offset1:224
	ds_read2_b32 v[26:27], v87 offset0:0 offset1:32
	ds_read2_b32 v[28:29], v87 offset0:64 offset1:96
	ds_read2_b32 v[30:31], v87 offset0:128 offset1:160
	ds_read2_b32 v[32:33], v87 offset0:192 offset1:224
	s_waitcnt lgkmcnt(0)
	v_max3_f32 v48, v18, v19, v20
	v_max3_f32 v50, v21, v22, v23
	v_max3_f32 v48, v48, v24, v25
	v_max3_f32 v50, v50, v26, v27
	v_max3_f32 v48, v48, v28, v29
	v_max3_f32 v50, v50, v30, v31
	v_max3_f32 v48, v48, v32, v33
	v_max_f32_e32 v48, v48, v50
	v_mov_b32_e32 v50, v48
	s_nop 1
	v_permlane32_swap_b32_e32 v48, v50
	v_max_f32_e32 v48, v48, v50
	v_fmamk_f32 v48, v48, 0x3fb8aa3b, v34
	v_pk_fma_f32 v[18:19], v[18:19], v[84:85], v[48:49] op_sel_hi:[1,0,0] neg_lo:[0,0,1] neg_hi:[0,0,1]
	v_exp_f32_e32 v18, v18
	v_exp_f32_e32 v19, v19
	v_pk_fma_f32 v[20:21], v[20:21], v[84:85], v[48:49] op_sel_hi:[1,0,0] neg_lo:[0,0,1] neg_hi:[0,0,1]
	v_exp_f32_e32 v20, v20
	v_exp_f32_e32 v21, v21
	v_pk_fma_f32 v[22:23], v[22:23], v[84:85], v[48:49] op_sel_hi:[1,0,0] neg_lo:[0,0,1] neg_hi:[0,0,1]
	v_exp_f32_e32 v22, v22
	v_exp_f32_e32 v23, v23
	v_pk_fma_f32 v[24:25], v[24:25], v[84:85], v[48:49] op_sel_hi:[1,0,0] neg_lo:[0,0,1] neg_hi:[0,0,1]
	v_exp_f32_e32 v24, v24
	v_exp_f32_e32 v25, v25
	v_pk_fma_f32 v[26:27], v[26:27], v[84:85], v[48:49] op_sel_hi:[1,0,0] neg_lo:[0,0,1] neg_hi:[0,0,1]
	v_exp_f32_e32 v26, v26
	v_exp_f32_e32 v27, v27
	v_pk_fma_f32 v[28:29], v[28:29], v[84:85], v[48:49] op_sel_hi:[1,0,0] neg_lo:[0,0,1] neg_hi:[0,0,1]
	v_exp_f32_e32 v28, v28
	v_exp_f32_e32 v29, v29
	v_pk_fma_f32 v[30:31], v[30:31], v[84:85], v[48:49] op_sel_hi:[1,0,0] neg_lo:[0,0,1] neg_hi:[0,0,1]
	v_exp_f32_e32 v30, v30
	v_exp_f32_e32 v31, v31
	v_pk_fma_f32 v[32:33], v[32:33], v[84:85], v[48:49] op_sel_hi:[1,0,0] neg_lo:[0,0,1] neg_hi:[0,0,1]
	v_exp_f32_e32 v32, v32
	v_exp_f32_e32 v33, v33
	v_pk_add_f32 v[56:57], v[18:19], v[20:21]
	v_pk_add_f32 v[58:59], v[22:23], v[24:25]
	v_pk_add_f32 v[60:61], v[26:27], v[28:29]
	v_pk_add_f32 v[62:63], v[30:31], v[32:33]
	v_pk_add_f32 v[56:57], v[56:57], v[58:59]
	v_pk_add_f32 v[60:61], v[60:61], v[62:63]
	v_pk_add_f32 v[56:57], v[56:57], v[60:61]
	v_add_f32_e32 v50, v56, v57
	v_mov_b32_e32 v51, v50
	s_nop 1
	v_permlane32_swap_b32_e32 v50, v51
	v_add_f32_e32 v50, v50, v51
	v_log_f32_e32 v50, v50
	v_cvt_pk_f16_f32 v40, v18, v19
	v_cvt_pk_f16_f32 v41, v20, v21
	v_cvt_pk_f16_f32 v42, v22, v23
	v_cvt_pk_f16_f32 v43, v24, v25
	v_cvt_pk_f16_f32 v44, v26, v27
	v_cvt_pk_f16_f32 v45, v28, v29
	v_cvt_pk_f16_f32 v46, v30, v31
	v_cvt_pk_f16_f32 v47, v32, v33
	v_add_f32_e32 v50, 0x41600000, v50
	v_mul_f32_e32 v50, 0xbf317218, v50
	v_cndmask_b32_e64 v51, v50, 1.0, vcc
	s_waitcnt vmcnt(0)
	ds_read_b128 v[2:5], v39
	ds_read_b128 v[6:9], v81
	ds_read_b128 v[10:13], v82
	ds_read_b128 v[14:17], v83
	s_waitcnt lgkmcnt(2)
	v_max3_f32 v52, v2, v3, v4
	v_max3_f32 v53, v5, v6, v7
	v_max_f32_e32 v52, v52, v8
	v_max_f32_e32 v53, v53, v9
	s_waitcnt lgkmcnt(0)
	v_max3_f32 v52, v52, v10, v11
	v_max3_f32 v53, v53, v12, v13
	v_max3_f32 v52, v52, v14, v15
	v_max3_f32 v53, v53, v16, v17
	v_max_f32_e32 v52, v52, v53
	v_mov_b32_e32 v53, v52
	s_nop 1
	v_permlane32_swap_b32_e32 v52, v53
	v_max_f32_e32 v52, v52, v53
	v_cndmask_b32_e32 v54, 1.0, v52, vcc
	v_fmamk_f32 v48, v52, 0x3fb8aa3b, v34
	v_pk_fma_f32 v[2:3], v[2:3], v[84:85], v[48:49] op_sel_hi:[1,0,0] neg_lo:[0,0,1] neg_hi:[0,0,1]
	v_mfma_f32_32x32x2_f32 v[64:79], v54, v51, 0
	v_exp_f32_e32 v2, v2
	v_exp_f32_e32 v3, v3
	v_pk_fma_f32 v[4:5], v[4:5], v[84:85], v[48:49] op_sel_hi:[1,0,0] neg_lo:[0,0,1] neg_hi:[0,0,1]
	v_exp_f32_e32 v4, v4
	v_exp_f32_e32 v5, v5
	v_pk_fma_f32 v[6:7], v[6:7], v[84:85], v[48:49] op_sel_hi:[1,0,0] neg_lo:[0,0,1] neg_hi:[0,0,1]
	v_exp_f32_e32 v6, v6
	v_exp_f32_e32 v7, v7
	v_pk_fma_f32 v[8:9], v[8:9], v[84:85], v[48:49] op_sel_hi:[1,0,0] neg_lo:[0,0,1] neg_hi:[0,0,1]
	v_exp_f32_e32 v8, v8
	v_exp_f32_e32 v9, v9
	v_pk_fma_f32 v[10:11], v[10:11], v[84:85], v[48:49] op_sel_hi:[1,0,0] neg_lo:[0,0,1] neg_hi:[0,0,1]
	v_exp_f32_e32 v10, v10
	v_cvt_pk_f16_f32 v56, v2, v3
	v_cvt_pk_f16_f32 v57, v4, v5
	v_cvt_pk_f16_f32 v58, v6, v7
	v_cvt_pk_f16_f32 v59, v8, v9
	v_exp_f32_e32 v11, v11
	v_pk_fma_f32 v[12:13], v[12:13], v[84:85], v[48:49] op_sel_hi:[1,0,0] neg_lo:[0,0,1] neg_hi:[0,0,1]
	v_exp_f32_e32 v12, v12
	v_mfma_f32_32x32x16_f16 v[18:33], v[56:59], v[40:43], 0
	v_exp_f32_e32 v13, v13
	v_pk_fma_f32 v[14:15], v[14:15], v[84:85], v[48:49] op_sel_hi:[1,0,0] neg_lo:[0,0,1] neg_hi:[0,0,1]
	v_exp_f32_e32 v14, v14
	v_exp_f32_e32 v15, v15
	v_pk_fma_f32 v[16:17], v[16:17], v[84:85], v[48:49] op_sel_hi:[1,0,0] neg_lo:[0,0,1] neg_hi:[0,0,1]
	v_exp_f32_e32 v16, v16
	v_exp_f32_e32 v17, v17
	v_cvt_pk_f16_f32 v60, v10, v11
	v_cvt_pk_f16_f32 v61, v12, v13
	v_cvt_pk_f16_f32 v62, v14, v15
	v_cvt_pk_f16_f32 v63, v16, v17
	s_nop 1
	v_mfma_f32_32x32x16_f16 v[18:33], v[60:63], v[44:47], v[18:33]
	s_nop 11
	v_log_f32_e32 v18, v18
	v_log_f32_e32 v19, v19
	v_log_f32_e32 v20, v20
	v_log_f32_e32 v21, v21
	v_log_f32_e32 v22, v22
	v_log_f32_e32 v23, v23
	v_pk_fma_f32 v[64:65], v[18:19], v[84:85], v[64:65] op_sel:[0,1,0] op_sel_hi:[1,1,1]
	buffer_store_dword v64, v36, s[8:11], 0 offen
	buffer_store_dword v65, v36, s[8:11], s24 offen
	v_log_f32_e32 v24, v24
	v_log_f32_e32 v25, v25
	v_pk_fma_f32 v[66:67], v[20:21], v[84:85], v[66:67] op_sel:[0,1,0] op_sel_hi:[1,1,1]
	buffer_store_dword v66, v36, s[8:11], s25 offen
	buffer_store_dword v67, v36, s[8:11], s26 offen
	v_log_f32_e32 v26, v26
	v_log_f32_e32 v27, v27
	v_pk_fma_f32 v[68:69], v[22:23], v[84:85], v[68:69] op_sel:[0,1,0] op_sel_hi:[1,1,1]
	buffer_store_dword v68, v36, s[8:11], s27 offen
	buffer_store_dword v69, v36, s[8:11], s28 offen
	v_log_f32_e32 v28, v28
	v_log_f32_e32 v29, v29
	v_pk_fma_f32 v[70:71], v[24:25], v[84:85], v[70:71] op_sel:[0,1,0] op_sel_hi:[1,1,1]
	buffer_store_dword v70, v36, s[8:11], s29 offen
	buffer_store_dword v71, v36, s[8:11], s30 offen
	v_log_f32_e32 v30, v30
	v_log_f32_e32 v31, v31
	v_pk_fma_f32 v[72:73], v[26:27], v[84:85], v[72:73] op_sel:[0,1,0] op_sel_hi:[1,1,1]
	buffer_store_dword v72, v36, s[8:11], s31 offen
	buffer_store_dword v73, v36, s[8:11], s32 offen
	v_log_f32_e32 v32, v32
	v_log_f32_e32 v33, v33
	v_pk_fma_f32 v[74:75], v[28:29], v[84:85], v[74:75] op_sel:[0,1,0] op_sel_hi:[1,1,1]
	buffer_store_dword v74, v36, s[8:11], s33 offen
	buffer_store_dword v75, v36, s[8:11], s34 offen
	v_pk_fma_f32 v[76:77], v[30:31], v[84:85], v[76:77] op_sel:[0,1,0] op_sel_hi:[1,1,1]
	buffer_store_dword v76, v36, s[8:11], s35 offen
	buffer_store_dword v77, v36, s[8:11], s36 offen
	v_pk_fma_f32 v[78:79], v[32:33], v[84:85], v[78:79] op_sel:[0,1,0] op_sel_hi:[1,1,1]
	buffer_store_dword v78, v36, s[8:11], s37 offen
	buffer_store_dword v79, v36, s[8:11], s38 offen
	s_endpgm
